# v_qk with loop head aligned to 64 bytes
# baseline (speedup 1.0000x reference)
_Z7k_fusedPKDF16_S0_S0_S0_PKfS2_S2_Pf:
	v_lshrrev_b32_e32 v222, 6, v0
	v_and_b32_e32 v1, 63, v0
	s_load_dwordx8 s[24:31], s[0:1], 0x8
	s_load_dwordx4 s[36:39], s[0:1], 0x28
	v_lshlrev_b32_e32 v4, 2, v222
	v_lshlrev_b32_e32 v5, 3, v1
	v_lshl_or_b32 v2, v222, 11, v5
	v_lshlrev_b32_e32 v224, 12, v222
	v_or_b32_e32 v6, 1, v4
	v_lshlrev_b32_e32 v223, 1, v2
	v_readfirstlane_b32 s3, v224
	v_lshl_or_b32 v2, v6, 9, v5
	v_lshlrev_b32_e32 v225, 10, v6
	v_mov_b32_e32 v211, 0
	s_mov_b32 m0, s3
	v_lshlrev_b32_e32 v210, 1, v2
	v_readfirstlane_b32 s3, v225
	s_waitcnt lgkmcnt(0)
	global_load_lds_dwordx4 v223, s[24:25]
	v_lshl_add_u64 v[2:3], s[24:25], 0, v[210:211]
	s_mov_b32 m0, s3
	v_or_b32_e32 v6, 2, v4
	global_load_lds_dwordx4 v[2:3], off
	v_lshl_or_b32 v2, v6, 9, v5
	v_lshlrev_b32_e32 v212, 1, v2
	v_mov_b32_e32 v213, v211
	v_lshl_add_u64 v[2:3], s[24:25], 0, v[212:213]
	v_lshlrev_b32_e32 v213, 10, v6
	v_or_b32_e32 v4, 3, v4
	v_readfirstlane_b32 s3, v213
	s_mov_b32 m0, s3
	v_mov_b32_e32 v215, v211
	global_load_lds_dwordx4 v[2:3], off
	v_lshl_or_b32 v2, v4, 9, v5
	v_lshlrev_b32_e32 v214, 1, v2
	v_lshl_add_u64 v[2:3], s[24:25], 0, v[214:215]
	v_lshlrev_b32_e32 v215, 10, v4
	s_nop 0
	v_readfirstlane_b32 s3, v215
	s_mov_b32 m0, s3
	s_movk_i32 s3, 0xff
	global_load_lds_dwordx4 v[2:3], off
	v_and_b32_e32 v2, 0x7f, v0
	v_lshlrev_b32_e32 v2, 2, v2
	global_load_dword v4, v2, s[36:37]
	global_load_dword v5, v2, s[38:39]
	s_lshl_b32 s3, s2, 8
	s_load_dwordx2 s[4:5], s[0:1], 0x0
	v_and_b32_e32 v6, 0xff, v0
	v_or_b32_e32 v6, s3, v6
	v_ashrrev_i32_e32 v7, 31, v6
	v_lshl_add_u64 v[6:7], v[6:7], 2, s[30:31]
	global_load_dword v244, v[6:7], off
	v_mov_b32_e32 v208, s3
	v_lshl_or_b32 v2, s2, 3, v222
	v_ashrrev_i32_e32 v3, 31, v2
	v_lshlrev_b64 v[2:3], 13, v[2:3]
	s_waitcnt lgkmcnt(0)
	v_lshl_add_u64 v[6:7], s[4:5], 0, v[2:3]
	v_mov_b32_e32 v2, 0
	v_lshlrev_b32_e32 v206, 4, v1
	v_mov_b32_e32 v207, v2
	v_lshl_add_u64 v[6:7], v[6:7], 0, v[206:207]
	v_lshlrev_b32_e32 v211, 13, v222
	v_ashrrev_i32_e32 v209, 31, v208
	v_lshl_add_u64 v[8:9], v[208:209], 2, s[30:31]
	v_or_b32_e32 v3, v211, v206
	v_lshl_add_u64 v[8:9], v[8:9], 0, v[206:207]
	global_load_dwordx4 v[68:71], v[8:9], off
	global_load_dwordx4 v[130:133], v[6:7], off
	global_load_dwordx4 v[134:137], v[6:7], off offset:1024
	global_load_dwordx4 v[138:141], v[6:7], off offset:2048
	global_load_dwordx4 v[142:145], v[6:7], off offset:3072
	s_movk_i32 s33, 0x1000
	v_add_co_u32_e32 v14, vcc, s33, v6
	s_nop 1
	v_addc_co_u32_e32 v15, vcc, 0, v7, vcc
	global_load_dwordx4 v[146:149], v[14:15], off
	global_load_dwordx4 v[150:153], v[14:15], off offset:1024
	global_load_dwordx4 v[154:157], v[14:15], off offset:2048
	global_load_dwordx4 v[158:161], v[14:15], off offset:3072
	v_lshlrev_b32_e32 v10, 1, v3
	global_load_dwordx4 v[186:189], v10, s[28:29] offset:16
	global_load_dwordx4 v[190:193], v10, s[28:29]
	global_load_dwordx4 v[178:181], v10, s[28:29] offset:2064
	global_load_dwordx4 v[182:185], v10, s[28:29] offset:2048
	v_mov_b32_e32 v11, v2
	v_lshl_add_u64 v[8:9], s[28:29], 0, v[10:11]
	v_add_co_u32_e32 v12, vcc, s33, v8
	s_mov_b64 s[34:35], 0x1000
	s_nop 0
	v_addc_co_u32_e32 v13, vcc, 0, v9, vcc
	s_mov_b64 s[40:41], 0x1800
	v_lshl_add_u64 v[10:11], v[8:9], 0, s[34:35]
	v_lshl_add_u64 v[8:9], v[8:9], 0, s[40:41]
	global_load_dwordx4 v[170:173], v[12:13], off
	global_load_dwordx4 v[174:177], v[10:11], off offset:16
	global_load_dwordx4 v[162:165], v[12:13], off offset:2048
	global_load_dwordx4 v[166:169], v[8:9], off offset:16
	s_waitcnt vmcnt(17)
	v_cmp_gt_u32_e32 vcc, 0x100, v0
	s_and_saveexec_b64 s[4:5], vcc
	v_lshlrev_b32_e32 v12, 4, v0
	v_and_b32_e32 v13, 0xe3, v0
	v_lshlrev_b32_e32 v14, 1, v0
	v_and_b32_e32 v12, 64, v12
	s_mov_b32 s8, 0x20000
	v_and_b32_e32 v14, 48, v14
	v_lshl_or_b32 v13, v13, 2, v12
	v_or3_b32 v13, v13, v14, s8
	v_add_f32_e32 v12, -1.0, v244
	v_mul_f32_e32 v12, 0x47000000, v12
	v_mul_f32_e32 v12, 0x3fb8aa3b, v12
	ds_write_b32 v13, v12
	s_or_b64 exec, exec, s[4:5]
	s_waitcnt lgkmcnt(0)
	s_barrier
	ds_read_b128 v[4:7], v206 offset:8192
	ds_read_b128 v[72:75], v206 offset:9216
	s_load_dwordx2 s[30:31], s[0:1], 0x38
	s_mov_b32 s0, 0x47000000
	s_mov_b32 s42, 0x3fb8aa3b
	s_mov_b32 s43, 0xff800000
	v_lshrrev_b32_e32 v96, 5, v1
	v_lshlrev_b32_e32 v97, 4, v96
	v_lshl_or_b32 v209, v222, 11, v206
	v_lshlrev_b32_e32 v1, 5, v1
	s_add_u32 s54, s24, 0x8000
	v_lshlrev_b32_e32 v207, 2, v96
	s_addc_u32 s55, s25, 0
	v_or_b32_e32 v227, 0x10000, v3
	s_mov_b32 s56, 0xc1d00000
	s_mov_b64 s[44:45], 0x20000
	s_mov_b64 s[46:47], 0x20800
	s_mov_b64 s[48:49], 0x21000
	s_mov_b32 s57, 0x21000
	s_mov_b64 s[50:51], 0x21800
	v_mov_b32_e32 v194, 0x3c003c00
	s_waitcnt lgkmcnt(0)
	s_waitcnt vmcnt(15)
	v_mfma_f32_32x32x16_f16 v[36:51], v[4:7], v[130:133], 0
	ds_read_b128 v[4:7], v206
	ds_read_b128 v[76:79], v206 offset:1024
	ds_read_b128 v[20:23], v206 offset:24576
	ds_read_b128 v[80:83], v206 offset:25600
	ds_read_b128 v[52:55], v206 offset:16384
	ds_read_b128 v[84:87], v206 offset:17408
	v_max_f32_e32 v71, v71, v71
	s_waitcnt lgkmcnt(1)
	v_mfma_f32_32x32x16_f16 v[52:67], v[130:133], v[52:55], 0
	v_max_f32_e32 v70, v70, v70
	v_max_f32_e32 v70, v70, v71
	s_waitcnt vmcnt(14)
	v_mfma_f32_32x32x16_f16 v[36:51], v[72:75], v[134:137], v[36:51]
	s_waitcnt lgkmcnt(0)
	v_mfma_f32_32x32x16_f16 v[52:67], v[134:137], v[84:87], v[52:67]
	ds_read_b128 v[72:75], v206 offset:10240
	ds_read_b128 v[84:87], v206 offset:11264
	s_waitcnt lgkmcnt(1)
	s_waitcnt vmcnt(13)
	v_mfma_f32_32x32x16_f16 v[36:51], v[72:75], v[138:141], v[36:51]
	ds_read_b128 v[72:75], v206 offset:18432
	ds_read_b128 v[88:91], v206 offset:19456
	s_waitcnt lgkmcnt(1)
	v_mfma_f32_32x32x16_f16 v[52:67], v[138:141], v[72:75], v[52:67]
	ds_read_b128 v[72:75], v206 offset:12288
	s_waitcnt vmcnt(12)
	v_mfma_f32_32x32x16_f16 v[36:51], v[84:87], v[142:145], v[36:51]
	v_mbcnt_lo_u32_b32 v84, -1, 0
	v_mbcnt_hi_u32_b32 v92, -1, v84
	ds_read_b128 v[84:87], v206 offset:13312
	v_xor_b32_e32 v93, 1, v92
	v_xor_b32_e32 v94, 2, v92
	v_xor_b32_e32 v95, 4, v92
	s_waitcnt lgkmcnt(2)
	v_mfma_f32_32x32x16_f16 v[52:67], v[142:145], v[88:91], v[52:67]
	v_and_b32_e32 v88, 64, v92
	v_add_u32_e32 v98, 64, v88
	v_cmp_lt_i32_e32 vcc, v93, v98
	ds_read_b128 v[88:91], v206 offset:21504
	s_waitcnt lgkmcnt(2)
	s_waitcnt vmcnt(11)
	v_mfma_f32_32x32x16_f16 v[36:51], v[72:75], v[146:149], v[36:51]
	ds_read_b128 v[72:75], v206 offset:20480
	s_waitcnt lgkmcnt(0)
	v_mfma_f32_32x32x16_f16 v[52:67], v[146:149], v[72:75], v[52:67]
	v_cndmask_b32_e32 v72, v92, v93, vcc
	v_lshlrev_b32_e32 v72, 2, v72
	v_max3_f32 v73, v68, v69, v70
	ds_bpermute_b32 v72, v72, v73
	v_cmp_lt_i32_e32 vcc, v94, v98
	s_waitcnt lgkmcnt(0)
	v_max_f32_e32 v72, v72, v72
	v_cndmask_b32_e32 v68, v92, v94, vcc
	v_lshlrev_b32_e32 v74, 2, v68
	ds_read_b128 v[68:71], v206 offset:14336
	s_waitcnt vmcnt(10)
	v_mfma_f32_32x32x16_f16 v[36:51], v[84:87], v[150:153], v[36:51]
	v_max_f32_e32 v84, v73, v72
	ds_bpermute_b32 v85, v74, v84
	v_cmp_lt_i32_e32 vcc, v95, v98
	s_waitcnt lgkmcnt(0)
	v_max_f32_e32 v85, v85, v85
	v_mfma_f32_32x32x16_f16 v[52:67], v[150:153], v[88:91], v[52:67]
	v_cndmask_b32_e32 v72, v92, v95, vcc
	v_lshlrev_b32_e32 v86, 2, v72
	v_max_f32_e32 v92, v84, v85
	ds_read_b128 v[72:75], v206 offset:15360
	ds_bpermute_b32 v93, v86, v92
	s_waitcnt lgkmcnt(0)
	v_max_f32_e32 v93, v93, v93
	s_waitcnt vmcnt(9)
	v_mfma_f32_32x32x16_f16 v[36:51], v[68:71], v[154:157], v[36:51]
	ds_read_b128 v[68:71], v206 offset:22528
	ds_read_b128 v[84:87], v206 offset:23552
	v_max_f32_e32 v92, v92, v93
	global_load_dwordx4 v[88:91], v97, s[36:37]
	v_readlane_b32 s3, v92, 0
	v_readlane_b32 s2, v92, 8
	v_readlane_b32 s5, v92, 16
	v_readlane_b32 s4, v92, 24
	s_waitcnt lgkmcnt(1)
	v_mfma_f32_32x32x16_f16 v[52:67], v[154:157], v[68:71], v[52:67]
	v_add_f32_e64 v68, s2, -1.0
	v_add_f32_e64 v69, s3, -1.0
	v_readlane_b32 s7, v92, 32
	v_readlane_b32 s6, v92, 40
	v_add_f32_e64 v70, s4, -1.0
	v_add_f32_e64 v71, s5, -1.0
	v_pk_mul_f32 v[68:69], v[68:69], s[0:1] op_sel_hi:[1,0]
	v_readlane_b32 s9, v92, 48
	v_readlane_b32 s8, v92, 56
	v_mfma_f32_32x32x16_f16 v[20:35], v[20:23], v[130:133], 0
	v_mul_f32_e64 v70, v70, s0
	v_mul_f32_e64 v71, v71, s0
	v_mul_f32_e64 v92, v68, s42
	v_mul_f32_e64 v93, v69, s42
	v_mul_f32_e64 v94, v70, s42
	v_mul_f32_e64 v95, v71, s42
	v_max3_f32 v68, v93, s43, v92
	v_max3_f32 v68, v68, v95, v94
	s_waitcnt vmcnt(9)
	v_mfma_f32_32x32x16_f16 v[36:51], v[72:75], v[158:161], v[36:51]
	v_add_f32_e64 v72, s6, -1.0
	v_add_f32_e64 v73, s7, -1.0
	v_mul_f32_e64 v72, v72, s0
	v_mul_f32_e64 v73, v73, s0
	s_waitcnt lgkmcnt(0)
	v_mfma_f32_32x32x16_f16 v[52:67], v[158:161], v[84:87], v[52:67]
	v_mul_f32_e64 v84, v72, s42
	v_mul_f32_e64 v85, v73, s42
	v_add_f32_e64 v86, s8, -1.0
	v_add_f32_e64 v87, s9, -1.0
	v_max3_f32 v98, v68, v85, v84
	ds_read_b128 v[68:71], v206 offset:26624
	v_cvt_pk_f16_f32 v43, v42, v43
	v_cvt_pk_f16_f32 v42, v40, v41
	v_cvt_pk_f16_f32 v41, v38, v39
	v_mfma_f32_32x32x16_f16 v[20:35], v[80:83], v[134:137], v[20:35]
	v_mul_f32_e64 v80, v86, s0
	v_mul_f32_e64 v81, v87, s0
	v_cvt_pk_f16_f32 v40, v36, v37
	v_mul_f32_e64 v86, v80, s42
	v_mul_f32_e64 v87, v81, s42
	global_load_dwordx4 v[72:75], v97, s[36:37] offset:32
	v_max3_f32 v80, v98, v87, v86
	v_add_f32_e32 v98, 0xc53b8000, v80
	ds_read_b128 v[80:83], v206 offset:27648
	global_load_dwordx4 v[36:39], v97, s[36:37] offset:64
	ds_write_b128 v209, v[40:43] offset:32768
	v_cvt_pk_f16_f32 v43, v50, v51
	v_cvt_pk_f16_f32 v40, v44, v45
	v_cvt_pk_f16_f32 v44, v52, v53
	global_load_dwordx4 v[50:53], v97, s[36:37] offset:96
	s_waitcnt lgkmcnt(2)
	v_mfma_f32_32x32x16_f16 v[20:35], v[68:71], v[138:141], v[20:35]
	ds_read_b128 v[68:71], v206 offset:28672
	v_cvt_pk_f16_f32 v42, v48, v49
	v_cvt_pk_f16_f32 v41, v46, v47
	ds_write_b128 v209, v[40:43] offset:33792
	ds_read_b128 v[40:43], v206 offset:30720
	v_cvt_pk_f16_f32 v47, v58, v59
	v_cvt_pk_f16_f32 v46, v56, v57
	s_waitcnt lgkmcnt(4)
	v_mfma_f32_32x32x16_f16 v[20:35], v[80:83], v[142:145], v[20:35]
	ds_read_b128 v[80:83], v206 offset:29696
	v_cvt_pk_f16_f32 v45, v54, v55
	ds_write_b128 v209, v[44:47] offset:49152
	v_cvt_pk_f16_f32 v45, v66, v67
	ds_read_b128 v[46:49], v206 offset:31744
	v_cvt_pk_f16_f32 v44, v64, v65
	v_cmp_ge_f32_e64 s[0:1], v92, v98
	s_waitcnt lgkmcnt(5)
	v_mfma_f32_32x32x16_f16 v[20:35], v[68:71], v[146:149], v[20:35]
	v_cmp_ge_f32_e64 s[2:3], v93, v98
	v_cmp_ge_f32_e64 s[4:5], v94, v98
	v_cmp_ge_f32_e64 s[6:7], v95, v98
	v_cmp_ge_f32_e64 s[8:9], v84, v98
	v_cmp_ge_f32_e64 s[10:11], v85, v98
	v_cmp_ge_f32_e64 s[12:13], v86, v98
	v_cmp_ge_f32_e64 s[14:15], v87, v98
	v_mfma_f32_32x32x16_f16 v[4:19], v[4:7], v[130:133], 0
	s_waitcnt lgkmcnt(2)
	v_mfma_f32_32x32x16_f16 v[20:35], v[80:83], v[150:153], v[20:35]
	v_mfma_f32_32x32x16_f16 v[4:19], v[76:79], v[134:137], v[4:19]
	v_mfma_f32_32x32x16_f16 v[20:35], v[40:43], v[154:157], v[20:35]
	v_cvt_pk_f16_f32 v43, v62, v63
	v_cvt_pk_f16_f32 v42, v60, v61
	ds_write_b128 v209, v[42:45] offset:50176
	ds_read_b128 v[40:43], v206 offset:2048
	ds_read_b128 v[54:57], v206 offset:3072
	s_waitcnt lgkmcnt(1)
	v_mfma_f32_32x32x16_f16 v[4:19], v[40:43], v[138:141], v[4:19]
	s_waitcnt lgkmcnt(0)
	v_mfma_f32_32x32x16_f16 v[4:19], v[54:57], v[142:145], v[4:19]
	v_mfma_f32_32x32x16_f16 v[20:35], v[46:49], v[158:161], v[20:35]
	ds_read_b128 v[44:47], v206 offset:4096
	ds_read_b128 v[58:61], v206 offset:5120
	ds_read_b128 v[62:65], v206 offset:6144
	ds_read_b128 v[66:69], v206 offset:7168
	s_waitcnt lgkmcnt(0)
	s_barrier
	s_waitcnt vmcnt(3)
	s_nop 4
	v_add_f32_e32 v20, v20, v88
	v_mfma_f32_32x32x16_f16 v[4:19], v[44:47], v[146:149], v[4:19]
	v_add_f32_e32 v21, v89, v21
	v_add_f32_e32 v22, v90, v22
	v_add_f32_e32 v23, v91, v23
	s_waitcnt vmcnt(2)
	v_add_f32_e32 v24, v24, v72
	v_add_f32_e32 v25, v73, v25
	v_add_f32_e32 v26, v74, v26
	v_add_f32_e32 v27, v75, v27
	v_mfma_f32_32x32x16_f16 v[4:19], v[58:61], v[150:153], v[4:19]
	s_waitcnt vmcnt(1)
	v_add_f32_e32 v28, v28, v36
	v_add_f32_e32 v29, v37, v29
	v_add_f32_e32 v30, v38, v30
	v_add_f32_e32 v31, v39, v31
	s_waitcnt vmcnt(0)
	v_add_f32_e32 v32, v32, v50
	v_add_f32_e32 v33, v51, v33
	v_add_f32_e32 v34, v52, v34
	v_mfma_f32_32x32x16_f16 v[4:19], v[62:65], v[154:157], v[4:19]
	v_add_f32_e32 v35, v53, v35
	v_mul_f32_e32 v20, 0xbfb8aa3b, v20
	v_mul_f32_e32 v21, 0xbfb8aa3b, v21
	v_mul_f32_e32 v22, 0xbfb8aa3b, v22
	v_mul_f32_e32 v23, 0xbfb8aa3b, v23
	v_mul_f32_e32 v24, 0xbfb8aa3b, v24
	v_mul_f32_e32 v25, 0xbfb8aa3b, v25
	v_mfma_f32_32x32x16_f16 v[4:19], v[66:69], v[158:161], v[4:19]
	v_mul_f32_e32 v26, 0xbfb8aa3b, v26
	v_mul_f32_e32 v27, 0xbfb8aa3b, v27
	v_mul_f32_e32 v28, 0xbfb8aa3b, v28
	v_mul_f32_e32 v29, 0xbfb8aa3b, v29
	v_mul_f32_e32 v30, 0xbfb8aa3b, v30
	v_mul_f32_e32 v31, 0xbfb8aa3b, v31
	v_mul_f32_e32 v32, 0xbfb8aa3b, v32
	v_mul_f32_e32 v33, 0xbfb8aa3b, v33
	v_mul_f32_e32 v34, 0xbfb8aa3b, v34
	v_mul_f32_e32 v35, 0xbfb8aa3b, v35
	v_exp_f32_e32 v20, v20
	v_exp_f32_e32 v21, v21
	v_exp_f32_e32 v22, v22
	v_exp_f32_e32 v23, v23
	v_exp_f32_e32 v24, v24
	v_exp_f32_e32 v25, v25
	v_exp_f32_e32 v26, v26
	v_exp_f32_e32 v27, v27
	v_exp_f32_e32 v28, v28
	v_exp_f32_e32 v29, v29
	v_exp_f32_e32 v30, v30
	v_exp_f32_e32 v31, v31
	v_exp_f32_e32 v32, v32
	v_exp_f32_e32 v33, v33
	v_exp_f32_e32 v34, v34
	v_exp_f32_e32 v35, v35
	v_add_f32_e32 v20, 1.0, v20
	v_add_f32_e32 v21, 1.0, v21
	v_add_f32_e32 v22, 1.0, v22
	v_add_f32_e32 v23, 1.0, v23
	v_add_f32_e32 v24, 1.0, v24
	v_add_f32_e32 v25, 1.0, v25
	v_add_f32_e32 v26, 1.0, v26
	v_add_f32_e32 v27, 1.0, v27
	v_add_f32_e32 v28, 1.0, v28
	v_add_f32_e32 v29, 1.0, v29
	v_add_f32_e32 v30, 1.0, v30
	v_add_f32_e32 v31, 1.0, v31
	v_add_f32_e32 v32, 1.0, v32
	v_add_f32_e32 v33, 1.0, v33
	v_add_f32_e32 v34, 1.0, v34
	v_add_f32_e32 v35, 1.0, v35
	v_rcp_f32_e32 v20, v20
	v_rcp_f32_e32 v21, v21
	v_rcp_f32_e32 v22, v22
	v_rcp_f32_e32 v23, v23
	v_rcp_f32_e32 v24, v24
	v_rcp_f32_e32 v25, v25
	v_rcp_f32_e32 v26, v26
	v_rcp_f32_e32 v27, v27
	v_rcp_f32_e32 v28, v28
	v_rcp_f32_e32 v29, v29
	v_rcp_f32_e32 v30, v30
	v_rcp_f32_e32 v31, v31
	v_rcp_f32_e32 v32, v32
	v_rcp_f32_e32 v33, v33
	v_rcp_f32_e32 v34, v34
	v_rcp_f32_e32 v35, v35
	v_cvt_pk_f16_f32 v198, v4, v5
	v_lshl_or_b32 v4, v222, 14, v1
	v_mov_b32_e32 v5, v2
	v_lshl_add_u64 v[216:217], s[28:29], 0, v[4:5]
	v_or_b32_e32 v4, 0x2000, v4
	v_lshrrev_b32_e32 v1, 1, v0
	v_lshl_add_u64 v[218:219], s[28:29], 0, v[4:5]
	v_and_b32_e32 v4, 16, v1
	v_mov_b32_e32 v36, 0x20000
	v_lshl_add_u64 v[4:5], s[36:37], 0, v[4:5]
	s_mov_b64 s[28:29], 0x80
	v_lshl_or_b32 v226, v96, 6, v36
	v_cvt_pk_f16_f32 v199, v6, v7
	v_cvt_pk_f16_f32 v200, v8, v9
	v_cvt_pk_f16_f32 v201, v10, v11
	v_cvt_pk_f16_f32 v202, v12, v13
	v_cvt_pk_f16_f32 v203, v14, v15
	v_cvt_pk_f16_f32 v204, v16, v17
	v_cvt_pk_f16_f32 v205, v18, v19
	v_cvt_pk_f16_f32 v229, v20, v21
	v_cvt_pk_f16_f32 v230, v22, v23
	v_cvt_pk_f16_f32 v232, v24, v25
	v_cvt_pk_f16_f32 v234, v26, v27
	v_cvt_pk_f16_f32 v228, v28, v29
	v_cvt_pk_f16_f32 v231, v30, v31
	v_cvt_pk_f16_f32 v233, v32, v33
	v_cvt_pk_f16_f32 v235, v34, v35
	v_lshl_add_u64 v[220:221], v[4:5], 0, s[28:29]
	s_mov_b64 s[36:37], 0
	s_branch .LBB1_6
	.p2align	6
